# speedup vs baseline: 1.0118x; 1.0026x over previous
amdhsa.kernels:
  - .agpr_count:     0
    .args:
      - .actual_access:  read_only
        .address_space:  global
        .offset:         0
        .size:           8
        .value_kind:     global_buffer
      - .actual_access:  read_only
        .address_space:  global
        .offset:         8
        .size:           8
        .value_kind:     global_buffer
      - .actual_access:  read_only
        .address_space:  global
        .offset:         16
        .size:           8
        .value_kind:     global_buffer
      - .actual_access:  read_only
        .address_space:  global
        .offset:         24
        .size:           8
        .value_kind:     global_buffer
      - .actual_access:  read_only
        .address_space:  global
        .offset:         32
        .size:           8
        .value_kind:     global_buffer
      - .actual_access:  read_only
        .address_space:  global
        .offset:         40
        .size:           8
        .value_kind:     global_buffer
      - .actual_access:  read_only
        .address_space:  global
        .offset:         48
        .size:           8
        .value_kind:     global_buffer
      - .actual_access:  write_only
        .address_space:  global
        .offset:         56
        .size:           8
        .value_kind:     global_buffer
    .group_segment_fixed_size: 98304
    .kernarg_segment_align: 8
    .kernarg_segment_size: 64
    .language:       OpenCL C
    .language_version:
      - 2
      - 0
    .max_flat_workgroup_size: 512
    .name:           _Z11k_conv_mfmaPKDF16_PKDv8_DF16_PKfS5_S5_S5_S5_PDF16_
    .private_segment_fixed_size: 0
    .sgpr_count:     36
    .sgpr_spill_count: 0
    .symbol:         _Z11k_conv_mfmaPKDF16_PKDv8_DF16_PKfS5_S5_S5_S5_PDF16_.kd
    .uniform_work_group_size: 1
    .uses_dynamic_stack: false
    .vgpr_count:     173
    .vgpr_spill_count: 0
    .wavefront_size: 64
  - .agpr_count:     0
    .args:
      - .actual_access:  read_only
        .address_space:  global
        .offset:         0
        .size:           8
        .value_kind:     global_buffer
      - .actual_access:  read_only
        .address_space:  global
        .offset:         8
        .size:           8
        .value_kind:     global_buffer
      - .actual_access:  read_only
        .address_space:  global
        .offset:         16
        .size:           8
        .value_kind:     global_buffer
      - .actual_access:  write_only
        .address_space:  global
        .offset:         24
        .size:           8
        .value_kind:     global_buffer
    .group_segment_fixed_size: 25600
    .kernarg_segment_align: 8
    .kernarg_segment_size: 32
    .language:       OpenCL C
    .language_version:
      - 2
      - 0
    .max_flat_workgroup_size: 1024
    .name:           _Z12k_recon_mfmaPKDF16_PKDv8_DF16_PKfPf
    .private_segment_fixed_size: 0
    .sgpr_count:     25
    .sgpr_spill_count: 0
    .symbol:         _Z12k_recon_mfmaPKDF16_PKDv8_DF16_PKfPf.kd
    .uniform_work_group_size: 1
    .uses_dynamic_stack: false
    .vgpr_count:     84
    .vgpr_spill_count: 0
    .wavefront_size: 64
  - .agpr_count:     0
    .args:
      - .actual_access:  read_only
        .address_space:  global
        .offset:         0
        .size:           8
        .value_kind:     global_buffer
      - .actual_access:  read_only
        .address_space:  global
        .offset:         8
        .size:           8
        .value_kind:     global_buffer
      - .actual_access:  read_only
        .address_space:  global
        .offset:         16
        .size:           8
        .value_kind:     global_buffer
      - .actual_access:  write_only
        .address_space:  global
        .offset:         24
        .size:           8
        .value_kind:     global_buffer
      - .actual_access:  write_only
        .address_space:  global
        .offset:         32
        .size:           8
        .value_kind:     global_buffer
      - .actual_access:  write_only
        .address_space:  global
        .offset:         40
        .size:           8
        .value_kind:     global_buffer
      - .actual_access:  write_only
        .address_space:  global
        .offset:         48
        .size:           8
        .value_kind:     global_buffer
      - .actual_access:  write_only
        .address_space:  global
        .offset:         56
        .size:           8
        .value_kind:     global_buffer
      - .actual_access:  write_only
        .address_space:  global
        .offset:         64
        .size:           8
        .value_kind:     global_buffer
    .group_segment_fixed_size: 67600
    .kernarg_segment_align: 8
    .kernarg_segment_size: 72
    .language:       OpenCL C
    .language_version:
      - 2
      - 0
    .max_flat_workgroup_size: 512
    .name:           _Z11k_proj_mfmaPKDF16_PKDv8_DF16_PKfPfPS1_S6_PhS6_PDF16_
    .private_segment_fixed_size: 0
    .sgpr_count:     36
    .sgpr_spill_count: 0
    .symbol:         _Z11k_proj_mfmaPKDF16_PKDv8_DF16_PKfPfPS1_S6_PhS6_PDF16_.kd
    .uniform_work_group_size: 1
    .uses_dynamic_stack: false
    .vgpr_count:     155
    .vgpr_spill_count: 0
    .wavefront_size: 64
  - .agpr_count:     0
    .args:
      - .actual_access:  read_only
        .address_space:  global
        .offset:         0
        .size:           8
        .value_kind:     global_buffer
      - .actual_access:  read_only
        .address_space:  global
        .offset:         8
        .size:           8
        .value_kind:     global_buffer
      - .actual_access:  read_only
        .address_space:  global
        .offset:         16
        .size:           8
        .value_kind:     global_buffer
      - .actual_access:  read_only
        .address_space:  global
        .offset:         24
        .size:           8
        .value_kind:     global_buffer
      - .actual_access:  read_only
        .address_space:  global
        .offset:         32
        .size:           8
        .value_kind:     global_buffer
      - .actual_access:  read_only
        .address_space:  global
        .offset:         40
        .size:           8
        .value_kind:     global_buffer
      - .actual_access:  write_only
        .address_space:  global
        .offset:         48
        .size:           8
        .value_kind:     global_buffer
      - .actual_access:  write_only
        .address_space:  global
        .offset:         56
        .size:           8
        .value_kind:     global_buffer
      - .actual_access:  read_only
        .address_space:  global
        .offset:         64
        .size:           8
        .value_kind:     global_buffer
      - .actual_access:  read_only
        .address_space:  global
        .offset:         72
        .size:           8
        .value_kind:     global_buffer
      - .actual_access:  write_only
        .address_space:  global
        .offset:         80
        .size:           8
        .value_kind:     global_buffer
      - .actual_access:  write_only
        .address_space:  global
        .offset:         88
        .size:           8
        .value_kind:     global_buffer
    .group_segment_fixed_size: 65536
    .kernarg_segment_align: 8
    .kernarg_segment_size: 96
    .language:       OpenCL C
    .language_version:
      - 2
      - 0
    .max_flat_workgroup_size: 512
    .name:           _Z6k_attnPKDv8_DF16_PKfPKhS3_S3_S3_PfS6_S3_S3_PS_S7_
    .private_segment_fixed_size: 0
    .sgpr_count:     34
    .sgpr_spill_count: 0
    .symbol:         _Z6k_attnPKDv8_DF16_PKfPKhS3_S3_S3_PfS6_S3_S3_PS_S7_.kd
    .uniform_work_group_size: 1
    .uses_dynamic_stack: false
    .vgpr_count:     128
    .vgpr_spill_count: 0
    .wavefront_size: 64
  - .agpr_count:     8
    .args:
      - .actual_access:  read_only
        .address_space:  global
        .offset:         0
        .size:           8
        .value_kind:     global_buffer
      - .actual_access:  read_only
        .address_space:  global
        .offset:         8
        .size:           8
        .value_kind:     global_buffer
      - .actual_access:  read_only
        .address_space:  global
        .offset:         16
        .size:           8
        .value_kind:     global_buffer
      - .actual_access:  read_only
        .address_space:  global
        .offset:         24
        .size:           8
        .value_kind:     global_buffer
      - .actual_access:  read_only
        .address_space:  global
        .offset:         32
        .size:           8
        .value_kind:     global_buffer
      - .actual_access:  write_only
        .address_space:  global
        .offset:         40
        .size:           8
        .value_kind:     global_buffer
    .group_segment_fixed_size: 10560
    .kernarg_segment_align: 8
    .kernarg_segment_size: 48
    .language:       OpenCL C
    .language_version:
      - 2
      - 0
    .max_flat_workgroup_size: 256
    .name:           _Z8k_resid2PKDF16_PKfS0_S2_S2_PDF16_
    .private_segment_fixed_size: 0
    .sgpr_count:     38
    .sgpr_spill_count: 0
    .symbol:         _Z8k_resid2PKDF16_PKfS0_S2_S2_PDF16_.kd
    .uniform_work_group_size: 1
    .uses_dynamic_stack: false
    .vgpr_count:     120
    .vgpr_spill_count: 0
    .wavefront_size: 64
  - .agpr_count:     0
    .args:
      - .actual_access:  read_only
        .address_space:  global
        .offset:         0
        .size:           8
        .value_kind:     global_buffer
      - .actual_access:  read_only
        .address_space:  global
        .offset:         8
        .size:           8
        .value_kind:     global_buffer
      - .actual_access:  read_only
        .address_space:  global
        .offset:         16
        .size:           8
        .value_kind:     global_buffer
      - .actual_access:  read_only
        .address_space:  global
        .offset:         24
        .size:           8
        .value_kind:     global_buffer
      - .actual_access:  read_only
        .address_space:  global
        .offset:         32
        .size:           8
        .value_kind:     global_buffer
      - .actual_access:  read_only
        .address_space:  global
        .offset:         40
        .size:           8
        .value_kind:     global_buffer
      - .actual_access:  read_only
        .address_space:  global
        .offset:         48
        .size:           8
        .value_kind:     global_buffer
      - .actual_access:  read_only
        .address_space:  global
        .offset:         56
        .size:           8
        .value_kind:     global_buffer
      - .actual_access:  read_only
        .address_space:  global
        .offset:         64
        .size:           8
        .value_kind:     global_buffer
      - .actual_access:  read_only
        .address_space:  global
        .offset:         72
        .size:           8
        .value_kind:     global_buffer
      - .actual_access:  write_only
        .address_space:  global
        .offset:         80
        .size:           8
        .value_kind:     global_buffer
      - .actual_access:  read_only
        .address_space:  global
        .offset:         88
        .size:           8
        .value_kind:     global_buffer
      - .actual_access:  read_only
        .address_space:  global
        .offset:         96
        .size:           8
        .value_kind:     global_buffer
      - .actual_access:  read_only
        .address_space:  global
        .offset:         104
        .size:           8
        .value_kind:     global_buffer
      - .actual_access:  read_only
        .address_space:  global
        .offset:         112
        .size:           8
        .value_kind:     global_buffer
      - .actual_access:  read_only
        .address_space:  global
        .offset:         120
        .size:           8
        .value_kind:     global_buffer
      - .actual_access:  read_only
        .address_space:  global
        .offset:         128
        .size:           8
        .value_kind:     global_buffer
      - .actual_access:  write_only
        .address_space:  global
        .offset:         136
        .size:           8
        .value_kind:     global_buffer
    .group_segment_fixed_size: 21248
    .kernarg_segment_align: 8
    .kernarg_segment_size: 144
    .language:       OpenCL C
    .language_version:
      - 2
      - 0
    .max_flat_workgroup_size: 512
    .name:           _Z8k_embed2PKfS0_S0_S0_S0_S0_S0_S0_S0_S0_PDF16_S0_S0_S0_S0_S0_S0_PDv8_DF16_
    .private_segment_fixed_size: 0
    .sgpr_count:     37
    .sgpr_spill_count: 0
    .symbol:         _Z8k_embed2PKfS0_S0_S0_S0_S0_S0_S0_S0_S0_PDF16_S0_S0_S0_S0_S0_S0_PDv8_DF16_.kd
    .uniform_work_group_size: 1
    .uses_dynamic_stack: false
    .vgpr_count:     99
    .vgpr_spill_count: 0
    .wavefront_size: 64
